# speedup vs baseline: 1.0076x; 1.0076x over previous
.LBB2_2:
	s_or_b64 exec, exec, s[4:5]
	v_cmp_gt_u32_e32 vcc, 64, v0
	s_waitcnt lgkmcnt(0)
	s_barrier
	s_and_saveexec_b64 s[4:5], vcc
	s_cbranch_execz .LBB2_5
	ds_read2st64_b32 v[4:5], v2 offset1:1
	ds_read2st64_b32 v[6:7], v2 offset0:2 offset1:3
	ds_read2st64_b32 v[8:9], v2 offset0:4 offset1:5
	ds_read2st64_b32 v[10:11], v2 offset0:6 offset1:7
	s_waitcnt lgkmcnt(3)
	v_max_f32_e32 v3, v5, v5
	v_max_f32_e32 v4, v4, v4
	v_max_f32_e32 v3, v4, v3
	s_waitcnt lgkmcnt(2)
	v_max3_f32 v3, v3, v6, v7
	s_waitcnt lgkmcnt(1)
	v_max3_f32 v12, v3, v8, v9
	ds_read2st64_b32 v[4:5], v2 offset0:8 offset1:9
	ds_read2st64_b32 v[6:7], v2 offset0:10 offset1:11
	ds_read2st64_b32 v[8:9], v2 offset0:12 offset1:13
	ds_read2st64_b32 v[2:3], v2 offset0:14 offset1:15
	s_waitcnt lgkmcnt(4)
	v_max3_f32 v10, v12, v10, v11
	s_waitcnt lgkmcnt(3)
	v_max3_f32 v4, v10, v4, v5
	s_waitcnt lgkmcnt(2)
	v_max3_f32 v4, v4, v6, v7
	s_waitcnt lgkmcnt(1)
	v_max3_f32 v4, v4, v8, v9
	s_waitcnt lgkmcnt(0)
	v_max3_f32 v2, v4, v2, v3
	v_add_f32_e32 v2, v39, v2
	v_mul_f32_e32 v4, v34, v2
	v_mul_f32_e32 v5, v35, v2
	s_nop 1
	v_add_f32_dpp v4, v4, v4 quad_perm:[1,0,3,2] row_mask:0xf bank_mask:0xf
	v_add_f32_dpp v5, v5, v5 quad_perm:[1,0,3,2] row_mask:0xf bank_mask:0xf
	s_nop 1
	v_add_f32_dpp v4, v4, v4 quad_perm:[2,3,0,1] row_mask:0xf bank_mask:0xf
	v_add_f32_dpp v5, v5, v5 quad_perm:[2,3,0,1] row_mask:0xf bank_mask:0xf
	s_nop 1
	v_add_f32_dpp v4, v4, v4 row_half_mirror row_mask:0xf bank_mask:0xf
	v_add_f32_dpp v5, v5, v5 row_half_mirror row_mask:0xf bank_mask:0xf
	s_nop 1
	v_add_f32_dpp v4, v4, v4 row_mirror row_mask:0xf bank_mask:0xf
	v_add_f32_dpp v5, v5, v5 row_mirror row_mask:0xf bank_mask:0xf
	s_nop 1
	v_readlane_b32 s4, v4, 16
	v_readlane_b32 s5, v4, 32
	v_readlane_b32 s6, v4, 48
	v_readlane_b32 s7, v5, 16
	v_readlane_b32 s12, v5, 32
	v_readlane_b32 s13, v5, 48
	s_lshl_b32 s0, s2, 1
	s_ashr_i32 s1, s0, 31
	s_lshl_b64 s[0:1], s[0:1], 2
	v_add_f32_e32 v4, s4, v4
	v_add_f32_e32 v5, s7, v5
	v_add_f32_e32 v4, s5, v4
	v_add_f32_e32 v5, s12, v5
	v_add_f32_e32 v4, s6, v4
	v_add_f32_e32 v5, s13, v5
	s_add_u32 s0, s22, s0
	s_addc_u32 s1, s23, s1
	v_cmp_eq_u32_e32 vcc, 0, v0
	s_and_b64 exec, exec, vcc
	s_cbranch_execz .LBB2_5
	v_mov_b32_e32 v6, 0
	s_waitcnt vmcnt(0)
	v_add_f32_e32 v0, v62, v4
	v_add_f32_e32 v1, v63, v5
	global_store_dwordx2 v6, v[0:1], s[0:1] sc0 sc1
